# baseline (speedup 1.0000x reference)
_Z11edge_kernelILi36ELb1EEvPKfS1_PKDF16_PKiS5_S1_S1_S1_S1_S1_PDF16_:
	s_load_dwordx4 s[4:7], s[0:1], 0x38
	s_load_dwordx2 s[8:9], s[0:1], 0x28
	s_load_dwordx2 s[10:11], s[0:1], 0x48
	v_lshlrev_b32_e32 v136, 4, v0
	v_mov_b32_e32 v137, 0
	v_readfirstlane_b32 s3, v0
	s_and_b32 s22, s2, 7
	s_lshr_b32 s23, s2, 3
	s_mul_i32 s22, s22, 0x271
	s_add_i32 s2, s22, s23
	s_lshl_b32 s2, s2, 1
	s_waitcnt lgkmcnt(0)
	v_lshl_add_u64 v[2:3], s[10:11], 0, v[136:137]
	global_load_dwordx4 v[28:31], v136, s[10:11]
	global_load_dwordx4 v[70:73], v136, s[10:11] offset:2048
	s_movk_i32 s10, 0x1000
	v_add_co_u32_e32 v4, vcc, s10, v2
	s_movk_i32 s10, 0x2000
	s_nop 0
	v_addc_co_u32_e32 v5, vcc, 0, v3, vcc
	s_lshr_b32 s16, s3, 6
	v_add_co_u32_e32 v6, vcc, s10, v2
	s_add_i32 s2, s16, s2
	v_lshrrev_b32_e32 v1, 4, v0
	v_addc_co_u32_e32 v7, vcc, 0, v3, vcc
	s_movk_i32 s10, 0x3000
	s_ashr_i32 s3, s2, 31
	s_mul_i32 s11, s2, 0x2400
	v_and_b32_e32 v78, 3, v1
	v_add_co_u32_e32 v2, vcc, s10, v2
	s_mul_hi_i32 s10, s2, 0x2400
	s_add_u32 s8, s8, s11
	v_and_b32_e32 v79, 15, v0
	s_addc_u32 s9, s9, s10
	v_mul_u32_u24_e32 v0, 0x90, v78
	v_mov_b32_e32 v1, v137
	v_lshl_add_u64 v[0:1], v[0:1], 4, s[8:9]
	s_lshl_b64 s[8:9], s[2:3], 14
	v_addc_co_u32_e32 v3, vcc, 0, v3, vcc
	s_add_u32 s4, s4, s8
	global_load_dwordx4 v[74:77], v[6:7], off offset:-4096
	global_load_dwordx4 v[80:83], v[6:7], off
	global_load_dwordx4 v[84:87], v[6:7], off offset:2048
	global_load_dwordx4 v[88:91], v[4:5], off offset:2048
	global_load_dwordx4 v[92:95], v[2:3], off
	global_load_dwordx4 v[96:99], v[2:3], off offset:2048
	v_lshlrev_b32_e32 v68, 4, v79
	v_mov_b32_e32 v69, v137
	s_addc_u32 s5, s5, s9
	v_lshlrev_b32_e32 v2, 12, v78
	v_mov_b32_e32 v3, v137
	v_lshl_add_u64 v[0:1], v[0:1], 0, v[68:69]
	v_lshl_add_u64 v[2:3], s[4:5], 0, v[2:3]
	global_load_dwordx4 v[100:103], v[0:1], off nt
	global_load_dwordx4 v[104:107], v[0:1], off offset:256 nt
	global_load_dwordx4 v[108:111], v[0:1], off offset:512 nt
	global_load_dwordx4 v[112:115], v[0:1], off offset:768 nt
	global_load_dwordx4 v[116:119], v[0:1], off offset:1024 nt
	global_load_dwordx4 v[120:123], v[0:1], off offset:1280 nt
	global_load_dwordx4 v[124:127], v[0:1], off offset:1536 nt
	global_load_dwordx4 v[128:131], v[0:1], off offset:1792 nt
	global_load_dwordx4 v[132:135], v[0:1], off offset:2048 nt
	v_lshl_add_u64 v[0:1], v[2:3], 0, v[68:69]
	global_load_dwordx4 v[60:63], v[0:1], off nt
	global_load_dwordx4 v[64:67], v[0:1], off offset:256 nt
	global_load_dwordx4 v[56:59], v[0:1], off offset:512 nt
	global_load_dwordx4 v[52:55], v[0:1], off offset:768 nt
	global_load_dwordx4 v[44:47], v[0:1], off offset:1024 nt
	global_load_dwordx4 v[48:51], v[0:1], off offset:1280 nt
	global_load_dwordx4 v[40:43], v[0:1], off offset:1536 nt
	global_load_dwordx4 v[36:39], v[0:1], off offset:1792 nt
	global_load_dwordx4 v[24:27], v[0:1], off offset:2048 nt
	global_load_dwordx4 v[32:35], v[0:1], off offset:2304 nt
	global_load_dwordx4 v[20:23], v[0:1], off offset:2560 nt
	global_load_dwordx4 v[16:19], v[0:1], off offset:2816 nt
	global_load_dwordx4 v[8:11], v[0:1], off offset:3072 nt
	global_load_dwordx4 v[12:15], v[0:1], off offset:3328 nt
	global_load_dwordx4 v[4:7], v[0:1], off offset:3584 nt
	s_nop 0
	global_load_dwordx4 v[0:3], v[0:1], off offset:3840 nt
	s_load_dwordx4 s[8:11], s[0:1], 0x0
	s_load_dwordx4 s[12:15], s[0:1], 0x18
	s_load_dwordx2 s[18:19], s[0:1], 0x30
	v_mul_u32_u24_e32 v69, 9, v78
	s_lshl_b64 s[4:5], s[2:3], 2
	s_waitcnt lgkmcnt(0)
	s_add_u32 s12, s12, s4
	s_waitcnt vmcnt(32)
	ds_write_b128 v136, v[28:31]
	s_waitcnt vmcnt(31)
	ds_write_b128 v136, v[70:73] offset:2048
	s_waitcnt vmcnt(30)
	ds_write_b128 v136, v[74:77] offset:4096
	s_waitcnt vmcnt(27)
	ds_write_b128 v136, v[88:91] offset:6144
	s_addc_u32 s13, s13, s5
	s_load_dword s12, s[12:13], 0x0
	ds_write_b128 v136, v[80:83] offset:8192
	ds_write_b128 v136, v[84:87] offset:10240
	s_waitcnt vmcnt(26)
	ds_write_b128 v136, v[92:95] offset:12288
	s_waitcnt vmcnt(25)
	ds_write_b128 v136, v[96:99] offset:14336
	v_lshlrev_b32_e32 v136, 2, v69
	v_cmp_eq_u32_e32 vcc, 3, v78
	v_mbcnt_lo_u32_b32 v69, -1, 0
	s_waitcnt lgkmcnt(0)
	s_ashr_i32 s13, s12, 31
	s_add_u32 s4, s14, s4
	s_addc_u32 s5, s15, s5
	s_lshl_b64 s[14:15], s[2:3], 8
	s_add_u32 s18, s18, s14
	s_addc_u32 s19, s19, s15
	s_add_u32 s6, s6, s14
	s_addc_u32 s7, s7, s15
	s_lshl_b64 s[14:15], s[12:13], 4
	s_add_u32 s10, s10, s14
	s_addc_u32 s11, s11, s15
	s_lshl_b64 s[12:13], s[12:13], 7
	s_add_u32 s8, s8, s12
	s_addc_u32 s9, s9, s13
	global_load_dwordx4 v[70:73], v136, s[8:9] nt
	v_lshl_add_u64 v[30:31], s[10:11], 0, v[136:137]
	s_movk_i32 s10, 0xff94
	v_lshl_add_u64 v[28:29], s[8:9], 0, v[136:137]
	s_mov_b32 s11, -1
	v_lshl_add_u64 v[28:29], v[28:29], 0, 20
	v_lshl_add_u64 v[30:31], v[30:31], 0, s[10:11]
	v_cndmask_b32_e32 v81, v29, v31, vcc
	v_cndmask_b32_e32 v80, v28, v30, vcc
	global_load_dwordx4 v[74:77], v[80:81], off nt
	global_load_dword v82, v136, s[8:9] offset:16 nt
	global_load_dwordx4 v[96:99], v68, s[18:19] nt
	global_load_dwordx4 v[28:31], v68, s[6:7] nt
	v_mbcnt_hi_u32_b32 v69, -1, v69
	v_xor_b32_e32 v83, 32, v69
	v_and_b32_e32 v81, 64, v69
	v_xor_b32_e32 v80, 16, v69
	v_add_u32_e32 v81, 64, v81
	v_cmp_lt_i32_e32 vcc, v80, v81
	s_load_dword s4, s[4:5], 0x0
	s_lshl_b32 s5, s16, 8
	v_cndmask_b32_e32 v80, v69, v80, vcc
	v_lshlrev_b32_e32 v80, 2, v80
	v_cmp_lt_i32_e32 vcc, v83, v81
	s_waitcnt lgkmcnt(0)
	s_barrier
	v_cndmask_b32_e32 v69, v69, v83, vcc
	v_lshlrev_b32_e32 v69, 2, v69
	s_addk_i32 s5, 0x4000
	v_cmp_eq_u32_e32 vcc, 0, v78
	v_lshl_add_u32 v81, v79, 4, s5
	s_waitcnt vmcnt(4)
	v_pk_fma_f32 v[84:85], v[70:71], v[102:103], 0 op_sel_hi:[0,1,0]
	v_pk_fma_f32 v[86:87], v[70:71], v[100:101], 0 op_sel_hi:[0,1,0]
	v_pk_fma_f32 v[86:87], v[70:71], v[104:105], v[86:87] op_sel:[1,0,0]
	v_pk_fma_f32 v[70:71], v[70:71], v[106:107], v[84:85] op_sel:[1,0,0]
	v_mov_b32_e32 v88, v73
	v_pk_fma_f32 v[70:71], v[72:73], v[110:111], v[70:71] op_sel_hi:[0,1,1]
	v_pk_fma_f32 v[72:73], v[72:73], v[108:109], v[86:87] op_sel_hi:[0,1,1]
	v_pk_fma_f32 v[72:73], v[88:89], v[112:113], v[72:73] op_sel_hi:[0,1,1]
	v_pk_fma_f32 v[70:71], v[88:89], v[114:115], v[70:71] op_sel_hi:[0,1,1]
	s_waitcnt vmcnt(2)
	v_pk_fma_f32 v[70:71], v[82:83], v[118:119], v[70:71] op_sel_hi:[0,1,1]
	v_pk_fma_f32 v[72:73], v[82:83], v[116:117], v[72:73] op_sel_hi:[0,1,1]
	v_pk_fma_f32 v[72:73], v[74:75], v[120:121], v[72:73] op_sel_hi:[0,1,1]
	v_pk_fma_f32 v[70:71], v[74:75], v[122:123], v[70:71] op_sel_hi:[0,1,1]
	v_pk_fma_f32 v[70:71], v[74:75], v[126:127], v[70:71] op_sel:[1,0,0]
	v_pk_fma_f32 v[72:73], v[74:75], v[124:125], v[72:73] op_sel:[1,0,0]
	v_mov_b32_e32 v84, v77
	v_pk_fma_f32 v[72:73], v[76:77], v[128:129], v[72:73] op_sel_hi:[0,1,1]
	v_pk_fma_f32 v[70:71], v[76:77], v[130:131], v[70:71] op_sel_hi:[0,1,1]
	v_pk_fma_f32 v[74:75], v[84:85], v[134:135], v[70:71] op_sel_hi:[0,1,1]
	v_pk_fma_f32 v[70:71], v[84:85], v[132:133], v[72:73] op_sel_hi:[0,1,1]
	ds_bpermute_b32 v72, v80, v70
	ds_bpermute_b32 v73, v80, v71
	ds_bpermute_b32 v76, v80, v74
	ds_bpermute_b32 v77, v80, v75
	s_waitcnt lgkmcnt(2)
	v_pk_add_f32 v[70:71], v[70:71], v[72:73]
	s_waitcnt lgkmcnt(0)
	v_pk_add_f32 v[72:73], v[74:75], v[76:77]
	ds_bpermute_b32 v76, v69, v70
	ds_bpermute_b32 v77, v69, v71
	ds_bpermute_b32 v74, v69, v72
	ds_bpermute_b32 v75, v69, v73
	s_and_saveexec_b64 s[6:7], vcc
	s_cbranch_execz .LBB2_2
	s_waitcnt lgkmcnt(0)
	v_pk_add_f32 v[70:71], v[70:71], v[76:77]
	v_pk_add_f32 v[72:73], v[72:73], v[74:75]
	s_waitcnt vmcnt(1)
	v_pk_add_f32 v[72:73], v[98:99], v[72:73]
	v_pk_add_f32 v[70:71], v[96:97], v[70:71]
	v_max_f32_e32 v72, 0, v72
	v_max_f32_e32 v70, 0, v70
	v_max_f32_e32 v71, 0, v71
	v_max_f32_e32 v73, 0, v73
	ds_write_b128 v81, v[70:73]

_Z11edge_kernelILi64ELb0EEvPKfS1_PKDF16_PKiS5_S1_S1_S1_S1_S1_PDF16_:
	s_load_dwordx8 s[4:11], s[0:1], 0x10
	s_load_dwordx4 s[12:15], s[0:1], 0x38
	s_load_dwordx2 s[16:17], s[0:1], 0x48
	s_load_dwordx2 s[20:21], s[0:1], 0x30
	v_lshlrev_b32_e32 v164, 4, v0
	v_mov_b32_e32 v165, 0
	v_readfirstlane_b32 s3, v0
	s_and_b32 s22, s2, 7
	s_lshr_b32 s23, s2, 3
	s_mul_i32 s22, s22, 0x271
	s_add_i32 s2, s22, s23
	s_lshl_b32 s2, s2, 1
	s_waitcnt lgkmcnt(0)
	v_lshl_add_u64 v[2:3], s[16:17], 0, v[164:165]
	global_load_dwordx4 v[128:131], v164, s[16:17]
	global_load_dwordx4 v[136:139], v164, s[16:17] offset:2048
	s_movk_i32 s16, 0x1000
	v_add_co_u32_e32 v4, vcc, s16, v2
	s_movk_i32 s16, 0x2000
	s_nop 0
	v_addc_co_u32_e32 v5, vcc, 0, v3, vcc
	v_add_co_u32_e32 v6, vcc, s16, v2
	s_movk_i32 s16, 0x3000
	s_nop 0
	v_addc_co_u32_e32 v7, vcc, 0, v3, vcc
	v_add_co_u32_e32 v2, vcc, s16, v2
	s_lshr_b32 s16, s3, 6
	s_add_i32 s2, s16, s2
	s_ashr_i32 s3, s2, 31
	s_lshl_b64 s[18:19], s[2:3], 14
	v_bfe_u32 v134, v0, 4, 2
	s_add_u32 s10, s10, s18
	v_addc_co_u32_e32 v3, vcc, 0, v3, vcc
	v_and_b32_e32 v135, 15, v0
	s_addc_u32 s11, s11, s19
	v_lshlrev_b32_e32 v0, 12, v134
	v_mov_b32_e32 v1, v165
	global_load_dwordx4 v[140:143], v[6:7], off offset:-4096
	global_load_dwordx4 v[144:147], v[6:7], off
	global_load_dwordx4 v[148:151], v[6:7], off offset:2048
	global_load_dwordx4 v[152:155], v[4:5], off offset:2048
	global_load_dwordx4 v[156:159], v[2:3], off
	global_load_dwordx4 v[160:163], v[2:3], off offset:2048
	v_lshl_add_u64 v[2:3], s[10:11], 0, v[0:1]
	s_add_u32 s10, s12, s18
	s_addc_u32 s11, s13, s19
	v_lshlrev_b32_e32 v132, 4, v135
	v_mov_b32_e32 v133, v165
	v_lshl_add_u64 v[0:1], s[10:11], 0, v[0:1]
	v_lshl_add_u64 v[2:3], v[2:3], 0, v[132:133]
	v_lshl_add_u64 v[0:1], v[0:1], 0, v[132:133]
	global_load_dwordx4 v[124:127], v[2:3], off nt
	global_load_dwordx4 v[120:123], v[2:3], off offset:256 nt
	global_load_dwordx4 v[116:119], v[2:3], off offset:512 nt
	global_load_dwordx4 v[112:115], v[2:3], off offset:768 nt
	global_load_dwordx4 v[108:111], v[2:3], off offset:1024 nt
	global_load_dwordx4 v[104:107], v[2:3], off offset:1280 nt
	global_load_dwordx4 v[100:103], v[2:3], off offset:1536 nt
	global_load_dwordx4 v[96:99], v[2:3], off offset:1792 nt
	global_load_dwordx4 v[92:95], v[2:3], off offset:2048 nt
	global_load_dwordx4 v[88:91], v[2:3], off offset:2304 nt
	global_load_dwordx4 v[84:87], v[2:3], off offset:2560 nt
	global_load_dwordx4 v[80:83], v[2:3], off offset:2816 nt
	global_load_dwordx4 v[76:79], v[2:3], off offset:3072 nt
	global_load_dwordx4 v[72:75], v[2:3], off offset:3328 nt
	global_load_dwordx4 v[68:71], v[2:3], off offset:3584 nt
	global_load_dwordx4 v[64:67], v[2:3], off offset:3840 nt
	global_load_dwordx4 v[56:59], v[0:1], off nt
	global_load_dwordx4 v[60:63], v[0:1], off offset:256 nt
	global_load_dwordx4 v[52:55], v[0:1], off offset:512 nt
	global_load_dwordx4 v[48:51], v[0:1], off offset:768 nt
	global_load_dwordx4 v[40:43], v[0:1], off offset:1024 nt
	global_load_dwordx4 v[44:47], v[0:1], off offset:1280 nt
	global_load_dwordx4 v[36:39], v[0:1], off offset:1536 nt
	global_load_dwordx4 v[32:35], v[0:1], off offset:1792 nt
	global_load_dwordx4 v[24:27], v[0:1], off offset:2048 nt
	global_load_dwordx4 v[28:31], v[0:1], off offset:2304 nt
	global_load_dwordx4 v[20:23], v[0:1], off offset:2560 nt
	global_load_dwordx4 v[16:19], v[0:1], off offset:2816 nt
	global_load_dwordx4 v[8:11], v[0:1], off offset:3072 nt
	global_load_dwordx4 v[12:15], v[0:1], off offset:3328 nt
	global_load_dwordx4 v[4:7], v[0:1], off offset:3584 nt
	s_nop 0
	global_load_dwordx4 v[0:3], v[0:1], off offset:3840 nt
	s_lshl_b64 s[10:11], s[2:3], 2
	s_add_u32 s6, s6, s10
	s_waitcnt vmcnt(39)
	ds_write_b128 v164, v[128:131]
	s_waitcnt vmcnt(38)
	ds_write_b128 v164, v[136:139] offset:2048
	s_waitcnt vmcnt(37)
	ds_write_b128 v164, v[140:143] offset:4096
	s_addc_u32 s7, s7, s11
	s_load_dword s12, s[6:7], 0x0
	v_lshlrev_b32_e32 v128, 5, v134
	s_waitcnt vmcnt(36)
	ds_write_b128 v164, v[144:147] offset:8192
	s_waitcnt vmcnt(34)
	ds_write_b128 v164, v[152:155] offset:6144
	s_waitcnt lgkmcnt(0)
	s_ashr_i32 s13, s12, 31
	s_add_u32 s6, s8, s10
	s_addc_u32 s7, s9, s11
	s_lshl_b64 s[8:9], s[2:3], 8
	s_add_u32 s20, s20, s8
	s_addc_u32 s21, s21, s9
	s_add_u32 s8, s14, s8
	s_addc_u32 s9, s15, s9
	s_lshl_b64 s[10:11], s[12:13], 7
	s_add_u32 s4, s4, s10
	s_addc_u32 s5, s5, s11
	global_load_dwordx4 v[138:141], v128, s[4:5] nt
	global_load_dwordx4 v[142:145], v128, s[4:5] offset:16 nt
	v_mbcnt_lo_u32_b32 v128, -1, 0
	v_mbcnt_hi_u32_b32 v128, -1, v128
	v_and_b32_e32 v130, 64, v128
	v_xor_b32_e32 v129, 16, v128
	v_add_u32_e32 v130, 64, v130
	v_xor_b32_e32 v131, 32, v128
	v_cmp_lt_i32_e32 vcc, v129, v130
	ds_write_b128 v164, v[148:151] offset:10240
	s_waitcnt vmcnt(35)
	ds_write_b128 v164, v[156:159] offset:12288
	s_waitcnt vmcnt(34)
	ds_write_b128 v164, v[160:163] offset:14336
	v_cndmask_b32_e32 v129, v128, v129, vcc
	v_cmp_lt_i32_e32 vcc, v131, v130
	v_lshlrev_b32_e32 v136, 2, v129
	s_load_dword s4, s[6:7], 0x0
	v_cndmask_b32_e32 v128, v128, v131, vcc
	v_lshlrev_b32_e32 v133, 2, v128
	global_load_dwordx4 v[156:159], v132, s[20:21] nt
	global_load_dwordx4 v[128:131], v132, s[8:9] nt
	s_lshl_b32 s5, s16, 8
	s_waitcnt lgkmcnt(0)
	s_barrier
	s_addk_i32 s5, 0x4000
	v_cmp_eq_u32_e32 vcc, 0, v134
	s_waitcnt vmcnt(3)
	v_cvt_f32_f16_e32 v137, v138
	v_cvt_f32_f16_sdwa v146, v138 dst_sel:DWORD dst_unused:UNUSED_PAD src0_sel:WORD_1
	v_cvt_f32_f16_e32 v147, v139
	v_cvt_f32_f16_sdwa v139, v139 dst_sel:DWORD dst_unused:UNUSED_PAD src0_sel:WORD_1
	v_cvt_f32_f16_e32 v150, v141
	v_cvt_f32_f16_sdwa v141, v141 dst_sel:DWORD dst_unused:UNUSED_PAD src0_sel:WORD_1
	v_cvt_f32_f16_e32 v148, v140
	s_waitcnt vmcnt(2)
	v_cvt_f32_f16_e32 v153, v143
	v_max_f32_e32 v138, 0, v137
	v_cvt_f32_f16_sdwa v137, v143 dst_sel:DWORD dst_unused:UNUSED_PAD src0_sel:WORD_1
	v_cvt_f32_f16_e32 v143, v144
	v_cvt_f32_f16_sdwa v149, v140 dst_sel:DWORD dst_unused:UNUSED_PAD src0_sel:WORD_1
	v_pk_fma_f32 v[126:127], v[138:139], v[126:127], 0 op_sel_hi:[0,1,0]
	v_pk_fma_f32 v[124:125], v[138:139], v[124:125], 0 op_sel_hi:[0,1,0]
	v_max_f32_e32 v138, 0, v146
	v_max_f32_e32 v140, 0, v147
	v_pk_fma_f32 v[122:123], v[138:139], v[122:123], v[126:127] op_sel_hi:[0,1,1]
	v_pk_fma_f32 v[120:121], v[138:139], v[120:121], v[124:125] op_sel_hi:[0,1,1]
	v_cvt_f32_f16_e32 v151, v142
	v_cvt_f32_f16_sdwa v152, v142 dst_sel:DWORD dst_unused:UNUSED_PAD src0_sel:WORD_1
	v_max_f32_e32 v142, 0, v139
	v_pk_fma_f32 v[116:117], v[140:141], v[116:117], v[120:121] op_sel_hi:[0,1,1]
	v_pk_fma_f32 v[118:119], v[140:141], v[118:119], v[122:123] op_sel_hi:[0,1,1]
	v_cvt_f32_f16_e32 v155, v145
	v_cvt_f32_f16_sdwa v145, v145 dst_sel:DWORD dst_unused:UNUSED_PAD src0_sel:WORD_1
	v_max_f32_e32 v124, 0, v148
	v_pk_fma_f32 v[114:115], v[142:143], v[114:115], v[118:119] op_sel_hi:[0,1,1]
	v_pk_fma_f32 v[112:113], v[142:143], v[112:113], v[116:117] op_sel_hi:[0,1,1]
	v_max_f32_e32 v126, 0, v149
	v_pk_fma_f32 v[108:109], v[124:125], v[108:109], v[112:113] op_sel_hi:[0,1,1]
	v_pk_fma_f32 v[110:111], v[124:125], v[110:111], v[114:115] op_sel_hi:[0,1,1]
	v_max_f32_e32 v138, 0, v150
	v_pk_fma_f32 v[106:107], v[126:127], v[106:107], v[110:111] op_sel_hi:[0,1,1]
	v_pk_fma_f32 v[104:105], v[126:127], v[104:105], v[108:109] op_sel_hi:[0,1,1]
	v_cvt_f32_f16_sdwa v154, v144 dst_sel:DWORD dst_unused:UNUSED_PAD src0_sel:WORD_1
	v_max_f32_e32 v144, 0, v141
	v_pk_fma_f32 v[100:101], v[138:139], v[100:101], v[104:105] op_sel_hi:[0,1,1]
	v_pk_fma_f32 v[102:103], v[138:139], v[102:103], v[106:107] op_sel_hi:[0,1,1]
	v_max_f32_e32 v146, 0, v151
	v_pk_fma_f32 v[98:99], v[144:145], v[98:99], v[102:103] op_sel_hi:[0,1,1]
	v_pk_fma_f32 v[96:97], v[144:145], v[96:97], v[100:101] op_sel_hi:[0,1,1]
	v_max_f32_e32 v148, 0, v152
	v_pk_fma_f32 v[92:93], v[146:147], v[92:93], v[96:97] op_sel_hi:[0,1,1]
	v_pk_fma_f32 v[94:95], v[146:147], v[94:95], v[98:99] op_sel_hi:[0,1,1]
	v_max_f32_e32 v120, 0, v153
	v_pk_fma_f32 v[90:91], v[148:149], v[90:91], v[94:95] op_sel_hi:[0,1,1]
	v_pk_fma_f32 v[88:89], v[148:149], v[88:89], v[92:93] op_sel_hi:[0,1,1]
	v_max_f32_e32 v122, 0, v137
	v_pk_fma_f32 v[84:85], v[120:121], v[84:85], v[88:89] op_sel_hi:[0,1,1]
	v_pk_fma_f32 v[86:87], v[120:121], v[86:87], v[90:91] op_sel_hi:[0,1,1]
	v_max_f32_e32 v140, 0, v143
	v_pk_fma_f32 v[82:83], v[122:123], v[82:83], v[86:87] op_sel_hi:[0,1,1]
	v_pk_fma_f32 v[80:81], v[122:123], v[80:81], v[84:85] op_sel_hi:[0,1,1]
	v_max_f32_e32 v150, 0, v154
	v_pk_fma_f32 v[76:77], v[140:141], v[76:77], v[80:81] op_sel_hi:[0,1,1]
	v_pk_fma_f32 v[78:79], v[140:141], v[78:79], v[82:83] op_sel_hi:[0,1,1]
	v_max_f32_e32 v152, 0, v155
	v_pk_fma_f32 v[74:75], v[150:151], v[74:75], v[78:79] op_sel_hi:[0,1,1]
	v_pk_fma_f32 v[72:73], v[150:151], v[72:73], v[76:77] op_sel_hi:[0,1,1]
	v_max_f32_e32 v154, 0, v145
	v_pk_fma_f32 v[68:69], v[152:153], v[68:69], v[72:73] op_sel_hi:[0,1,1]
	v_pk_fma_f32 v[70:71], v[152:153], v[70:71], v[74:75] op_sel_hi:[0,1,1]
	v_pk_fma_f32 v[66:67], v[154:155], v[66:67], v[70:71] op_sel_hi:[0,1,1]
	v_pk_fma_f32 v[64:65], v[154:155], v[64:65], v[68:69] op_sel_hi:[0,1,1]
	ds_bpermute_b32 v68, v136, v64
	ds_bpermute_b32 v69, v136, v65
	ds_bpermute_b32 v70, v136, v66
	ds_bpermute_b32 v71, v136, v67
	v_lshl_add_u32 v72, v135, 4, s5
	s_waitcnt lgkmcnt(2)
	v_pk_add_f32 v[64:65], v[64:65], v[68:69]
	s_waitcnt lgkmcnt(0)
	v_pk_add_f32 v[66:67], v[66:67], v[70:71]
	ds_bpermute_b32 v70, v133, v64
	ds_bpermute_b32 v71, v133, v65
	ds_bpermute_b32 v68, v133, v66
	ds_bpermute_b32 v69, v133, v67
	s_and_saveexec_b64 s[6:7], vcc
	s_cbranch_execz .LBB3_2
	s_waitcnt lgkmcnt(0)
	v_pk_add_f32 v[64:65], v[64:65], v[70:71]
	v_pk_add_f32 v[66:67], v[66:67], v[68:69]
	s_waitcnt vmcnt(1)
	v_pk_add_f32 v[66:67], v[158:159], v[66:67]
	v_pk_add_f32 v[64:65], v[156:157], v[64:65]
	v_max_f32_e32 v66, 0, v66
	v_max_f32_e32 v64, 0, v64
	v_max_f32_e32 v65, 0, v65
	v_max_f32_e32 v67, 0, v67
	ds_write_b128 v72, v[64:67]
